# P1/P4 side-job fast path trimmed: 32-bit job addresses (h*8448+lo, h<<15+lo), SADDR store and loads, 8 v_mul_f32 for 4 v_pk_mul_f32; 66-73 -> 47-54 instructions per job, two per bf16 MFMA gap
# baseline (speedup 1.0000x reference)
; #define PG8_LAS __attribute__((address_space(3)))
;     __device__ __forceinline__ void issue(PG8_LAS unsigned char* lds0, int j, int tid, int wid) const {
;         const float* s0; unsigned char* d; addr(j, tid, s0, d);
;         __builtin_amdgcn_global_load_lds((const unsigned*)s0, (PG8_LAS unsigned*)(lds0 + stage + wid * 1024), 16, 0, 2);
;         __builtin_amdgcn_global_load_lds((const unsigned*)(s0 + ntot), (PG8_LAS unsigned*)(lds0 + stage + 8192 + wid * 1024), 16, 0, 2);
;     }
;     __device__ __forceinline__ void read(v4i_t& t0, v4i_t& t1, int tid, unsigned ldsb) const {
;         asm volatile("ds_read_b128 %0, %1" : "=&v"(t0) : "v"(ldsb + stage + 16u * (unsigned)tid) : "memory");
;         asm volatile("ds_read_b128 %0, %1" : "=&v"(t1) : "v"(ldsb + stage + 8192u + 16u * (unsigned)tid) : "memory");
;     }
;     __device__ __forceinline__ void finish(v4i_t& t0, v4i_t& t1, int j, int tid) const {
;         asm volatile("" : "+v"(t0), "+v"(t1));
;         const float* s0; unsigned char* d; addr(j, tid, s0, d);
;         const f32x4 r0 = __builtin_bit_cast(f32x4, t0) * 64.f, r1 = __builtin_bit_cast(f32x4, t1) * 64.f;
;         int w0 = 0, w1 = 0; w0 = __builtin_amdgcn_cvt_pk_fp8_f32(r0[0], r1[0], w0, false); w0 = __builtin_amdgcn_cvt_pk_fp8_f32(r0[1], r1[1], w0, true);
;         w1 = __builtin_amdgcn_cvt_pk_fp8_f32(r0[2], r1[2], w1, false); w1 = __builtin_amdgcn_cvt_pk_fp8_f32(r0[3], r1[3], w1, true);
;         typedef int v2is __attribute__((ext_vector_type(2))); __builtin_nontemporal_store((v2is){w0, w1}, (v2is*)d);
.Lp1vg_wd_a1:
	s_waitcnt lgkmcnt(0)
	s_barrier
	s_cmp_lt_i32 s98, 0
	s_cbranch_scc1 .Lp1vg_mmslow_a
	s_cmpk_gt_i32 s77, 0x5f
	s_cbranch_scc1 .Lp1vg_mmslow_a
	s_setprio 1
	s_waitcnt lgkmcnt(0)
	v_mfma_f32_16x16x32_bf16 v[138:141], v[158:161], v[198:201], v[138:141]
	s_add_i32 s4, s98, s68
	s_lshr_b32 s5, s4, 1
	v_mfma_f32_16x16x32_bf16 v[134:137], v[166:169], v[198:201], v[134:137]
	s_and_b32 s4, s4, 1
	s_lshl_b32 s4, s4, 12
	v_mfma_f32_16x16x32_bf16 v[122:125], v[158:161], v[190:193], v[122:125]
	s_mulk_i32 s5, 0x2100
	s_add_i32 s4, s4, s5
	v_mfma_f32_16x16x32_bf16 v[118:121], v[166:169], v[190:193], v[118:121]
	v_mul_f32_e32 v6, s40, v6
	v_mul_f32_e32 v10, s40, v10
	v_mfma_f32_16x16x32_bf16 v[106:109], v[158:161], v[182:185], v[106:109]
	v_mul_f32_e32 v7, s40, v7
	v_mul_f32_e32 v11, s40, v11
	v_mfma_f32_16x16x32_bf16 v[102:105], v[166:169], v[182:185], v[102:105]
	v_cvt_pk_fp8_f32 v6, v6, v10
	v_mul_f32_e32 v8, s40, v8
	v_mfma_f32_16x16x32_bf16 v[90:93], v[158:161], v[174:177], v[90:93]
	v_mul_f32_e32 v12, s40, v12
	v_cvt_pk_fp8_f32 v6, v7, v11 op_sel:[0,0,1]
	v_mfma_f32_16x16x32_bf16 v[86:89], v[166:169], v[174:177], v[86:89]
	v_mul_f32_e32 v9, s40, v9
	v_mul_f32_e32 v13, s40, v13
	v_mfma_f32_16x16x32_bf16 v[138:141], v[162:165], v[202:205], v[138:141]
	v_readlane_b32 s2, v251, 49
	v_cvt_pk_fp8_f32 v7, v8, v12
	v_mfma_f32_16x16x32_bf16 v[134:137], v[170:173], v[202:205], v[134:137]
	v_readlane_b32 s3, v251, 31
	v_cvt_pk_fp8_f32 v7, v9, v13 op_sel:[0,0,1]
	v_mfma_f32_16x16x32_bf16 v[122:125], v[162:165], v[194:197], v[122:125]
	s_add_u32 s2, s2, s4
	s_addc_u32 s3, s3, 0
	v_mfma_f32_16x16x32_bf16 v[118:121], v[170:173], v[194:197], v[118:121]
	v_lshlrev_b32_e32 v4, 1, v208
	global_store_dwordx2 v4, v[6:7], s[2:3] nt
	v_mfma_f32_16x16x32_bf16 v[106:109], v[162:165], v[186:189], v[106:109]
	s_add_i32 s4, s77, s68
	s_lshr_b32 s5, s4, 1
	v_mfma_f32_16x16x32_bf16 v[102:105], v[170:173], v[186:189], v[102:105]
	s_and_b32 s4, s4, 1
	s_lshl_b32 s4, s4, 13
	v_mfma_f32_16x16x32_bf16 v[90:93], v[162:165], v[178:181], v[90:93]
	s_lshl_b32 s5, s5, 15
	s_add_i32 s4, s4, s5
	v_mfma_f32_16x16x32_bf16 v[86:89], v[170:173], v[178:181], v[86:89]
	s_setprio 0
	s_setprio 1
	v_readlane_b32 s2, v251, 36
	v_readlane_b32 s3, v251, 37
	v_mfma_f32_16x16x32_bf16 v[130:133], v[142:145], v[198:201], v[130:133]
	s_add_u32 s2, s2, s4
	s_addc_u32 s3, s3, 0
	v_mfma_f32_16x16x32_bf16 v[126:129], v[150:153], v[198:201], v[126:129]
	s_add_u32 s56, s2, s42
	s_addc_u32 s57, s3, s43
	v_mfma_f32_16x16x32_bf16 v[114:117], v[142:145], v[190:193], v[114:117]
	v_lshlrev_b32_e32 v2, 2, v208
	global_load_dwordx4 v[6:9], v2, s[2:3] nt
	v_mfma_f32_16x16x32_bf16 v[110:113], v[150:153], v[190:193], v[110:113]
	global_load_dwordx4 v[10:13], v2, s[56:57] nt
	s_mov_b32 s100, 3
	v_mfma_f32_16x16x32_bf16 v[98:101], v[142:145], v[182:185], v[98:101]
	s_mov_b32 s98, s77
	s_add_i32 s77, s77, 1
	v_mfma_f32_16x16x32_bf16 v[94:97], v[150:153], v[182:185], v[94:97]
	s_add_u32 s4, s54, 0xfff80080
	s_addc_u32 s5, s55, -1
	v_mfma_f32_16x16x32_bf16 v[82:85], v[142:145], v[174:177], v[82:85]
	s_cmp_eq_u32 s81, 28
	s_cselect_b32 s5, s7, s5
	s_cselect_b32 s4, s33, s4
	s_cselect_b32 s57, s45, s80
	s_cselect_b32 s56, s47, s79
	v_mfma_f32_16x16x32_bf16 v[78:81], v[150:153], v[174:177], v[78:81]
	v_mfma_f32_16x16x32_bf16 v[130:133], v[146:149], v[202:205], v[130:133]
	v_mfma_f32_16x16x32_bf16 v[126:129], v[154:157], v[202:205], v[126:129]
	v_mfma_f32_16x16x32_bf16 v[114:117], v[146:149], v[194:197], v[114:117]
	v_mfma_f32_16x16x32_bf16 v[110:113], v[154:157], v[194:197], v[110:113]
	v_mfma_f32_16x16x32_bf16 v[98:101], v[146:149], v[186:189], v[98:101]
	v_mfma_f32_16x16x32_bf16 v[94:97], v[154:157], v[186:189], v[94:97]
	v_mfma_f32_16x16x32_bf16 v[82:85], v[146:149], v[178:181], v[82:85]
	v_mfma_f32_16x16x32_bf16 v[78:81], v[154:157], v[178:181], v[78:81]
	s_setprio 0
	s_branch .Lp1vg_mmjoin_a

; #define PG8_LAS __attribute__((address_space(3)))
;     __device__ __forceinline__ void issue(PG8_LAS unsigned char* lds0, int j, int tid, int wid) const {
;         const float* s0; unsigned char* d; addr(j, tid, s0, d);
;         __builtin_amdgcn_global_load_lds((const unsigned*)s0, (PG8_LAS unsigned*)(lds0 + stage + wid * 1024), 16, 0, 2);
;         __builtin_amdgcn_global_load_lds((const unsigned*)(s0 + ntot), (PG8_LAS unsigned*)(lds0 + stage + 8192 + wid * 1024), 16, 0, 2);
;     }
;     __device__ __forceinline__ void read(v4i_t& t0, v4i_t& t1, int tid, unsigned ldsb) const {
;         asm volatile("ds_read_b128 %0, %1" : "=&v"(t0) : "v"(ldsb + stage + 16u * (unsigned)tid) : "memory");
;         asm volatile("ds_read_b128 %0, %1" : "=&v"(t1) : "v"(ldsb + stage + 8192u + 16u * (unsigned)tid) : "memory");
;     }
;     __device__ __forceinline__ void finish(v4i_t& t0, v4i_t& t1, int j, int tid) const {
;         asm volatile("" : "+v"(t0), "+v"(t1));
;         const float* s0; unsigned char* d; addr(j, tid, s0, d);
;         const f32x4 r0 = __builtin_bit_cast(f32x4, t0) * 64.f, r1 = __builtin_bit_cast(f32x4, t1) * 64.f;
;         int w0 = 0, w1 = 0; w0 = __builtin_amdgcn_cvt_pk_fp8_f32(r0[0], r1[0], w0, false); w0 = __builtin_amdgcn_cvt_pk_fp8_f32(r0[1], r1[1], w0, true);
;         w1 = __builtin_amdgcn_cvt_pk_fp8_f32(r0[2], r1[2], w1, false); w1 = __builtin_amdgcn_cvt_pk_fp8_f32(r0[3], r1[3], w1, true);
;         typedef int v2is __attribute__((ext_vector_type(2))); __builtin_nontemporal_store((v2is){w0, w1}, (v2is*)d);
.Lp1vg_wd_b1:
	s_waitcnt lgkmcnt(0)
	s_cmp_lt_i32 s99, 0
	s_cbranch_scc1 .Lp1vg_mmslow_b
	s_cmpk_gt_i32 s77, 0x5f
	s_cbranch_scc1 .Lp1vg_mmslow_b
	s_barrier
	s_setprio 1
	s_waitcnt lgkmcnt(0)
	v_mfma_f32_16x16x32_bf16 v[138:141], v[158:161], v[198:201], v[138:141]
	s_add_i32 s4, s99, s68
	s_lshr_b32 s5, s4, 1
	v_mfma_f32_16x16x32_bf16 v[134:137], v[166:169], v[198:201], v[134:137]
	s_and_b32 s4, s4, 1
	s_lshl_b32 s4, s4, 12
	v_mfma_f32_16x16x32_bf16 v[122:125], v[158:161], v[190:193], v[122:125]
	s_mulk_i32 s5, 0x2100
	s_add_i32 s4, s4, s5
	v_mfma_f32_16x16x32_bf16 v[118:121], v[166:169], v[190:193], v[118:121]
	v_mul_f32_e32 v240, s40, v240
	v_mul_f32_e32 v244, s40, v244
	v_mfma_f32_16x16x32_bf16 v[106:109], v[158:161], v[182:185], v[106:109]
	v_mul_f32_e32 v241, s40, v241
	v_mul_f32_e32 v245, s40, v245
	v_mfma_f32_16x16x32_bf16 v[102:105], v[166:169], v[182:185], v[102:105]
	v_cvt_pk_fp8_f32 v240, v240, v244
	v_mul_f32_e32 v242, s40, v242
	v_mfma_f32_16x16x32_bf16 v[90:93], v[158:161], v[174:177], v[90:93]
	v_mul_f32_e32 v246, s40, v246
	v_cvt_pk_fp8_f32 v240, v241, v245 op_sel:[0,0,1]
	v_mfma_f32_16x16x32_bf16 v[86:89], v[166:169], v[174:177], v[86:89]
	v_mul_f32_e32 v243, s40, v243
	v_mul_f32_e32 v247, s40, v247
	v_mfma_f32_16x16x32_bf16 v[138:141], v[162:165], v[202:205], v[138:141]
	v_readlane_b32 s2, v251, 49
	v_cvt_pk_fp8_f32 v241, v242, v246
	v_mfma_f32_16x16x32_bf16 v[134:137], v[170:173], v[202:205], v[134:137]
	v_readlane_b32 s3, v251, 31
	v_cvt_pk_fp8_f32 v241, v243, v247 op_sel:[0,0,1]
	v_mfma_f32_16x16x32_bf16 v[122:125], v[162:165], v[194:197], v[122:125]
	s_add_u32 s2, s2, s4
	s_addc_u32 s3, s3, 0
	v_mfma_f32_16x16x32_bf16 v[118:121], v[170:173], v[194:197], v[118:121]
	v_lshlrev_b32_e32 v238, 1, v208
	global_store_dwordx2 v238, v[240:241], s[2:3] nt
	v_mfma_f32_16x16x32_bf16 v[106:109], v[162:165], v[186:189], v[106:109]
	s_add_i32 s4, s77, s68
	s_lshr_b32 s5, s4, 1
	v_mfma_f32_16x16x32_bf16 v[102:105], v[170:173], v[186:189], v[102:105]
	s_and_b32 s4, s4, 1
	s_lshl_b32 s4, s4, 13
	v_mfma_f32_16x16x32_bf16 v[90:93], v[162:165], v[178:181], v[90:93]
	s_lshl_b32 s5, s5, 15
	s_add_i32 s4, s4, s5
	v_mfma_f32_16x16x32_bf16 v[86:89], v[170:173], v[178:181], v[86:89]
	s_setprio 0
	s_setprio 1
	v_readlane_b32 s2, v251, 36
	v_readlane_b32 s3, v251, 37
	v_mfma_f32_16x16x32_bf16 v[130:133], v[142:145], v[198:201], v[130:133]
	s_add_u32 s2, s2, s4
	s_addc_u32 s3, s3, 0
	v_mfma_f32_16x16x32_bf16 v[126:129], v[150:153], v[198:201], v[126:129]
	s_add_u32 s84, s2, s42
	s_addc_u32 s85, s3, s43
	v_mfma_f32_16x16x32_bf16 v[114:117], v[142:145], v[190:193], v[114:117]
	v_lshlrev_b32_e32 v2, 2, v208
	global_load_dwordx4 v[240:243], v2, s[2:3] nt
	v_mfma_f32_16x16x32_bf16 v[110:113], v[150:153], v[190:193], v[110:113]
	global_load_dwordx4 v[244:247], v2, s[84:85] nt
	s_mov_b32 s100, 3
	v_mfma_f32_16x16x32_bf16 v[98:101], v[142:145], v[182:185], v[98:101]
	s_mov_b32 s99, s77
	s_add_i32 s77, s77, 1
	v_mfma_f32_16x16x32_bf16 v[94:97], v[150:153], v[182:185], v[94:97]
	v_mfma_f32_16x16x32_bf16 v[82:85], v[142:145], v[174:177], v[82:85]
	v_mfma_f32_16x16x32_bf16 v[78:81], v[150:153], v[174:177], v[78:81]
	v_mfma_f32_16x16x32_bf16 v[130:133], v[146:149], v[202:205], v[130:133]
	v_mfma_f32_16x16x32_bf16 v[126:129], v[154:157], v[202:205], v[126:129]
	v_mfma_f32_16x16x32_bf16 v[114:117], v[146:149], v[194:197], v[114:117]
	v_mfma_f32_16x16x32_bf16 v[110:113], v[154:157], v[194:197], v[110:113]
	v_mfma_f32_16x16x32_bf16 v[98:101], v[146:149], v[186:189], v[98:101]
	v_mfma_f32_16x16x32_bf16 v[94:97], v[154:157], v[186:189], v[94:97]
	v_mfma_f32_16x16x32_bf16 v[82:85], v[146:149], v[178:181], v[82:85]
	v_mfma_f32_16x16x32_bf16 v[78:81], v[154:157], v[178:181], v[78:81]
	s_setprio 0
	s_branch .Lp1vg_mmafter_b

; #define PG8_LAS __attribute__((address_space(3)))
;     __device__ __forceinline__ void issue(PG8_LAS unsigned char* lds0, int j, int tid, int wid) const {
;         const float* s0; unsigned char* d; addr(j, tid, s0, d);
;         __builtin_amdgcn_global_load_lds((const unsigned*)s0, (PG8_LAS unsigned*)(lds0 + stage + wid * 1024), 16, 0, 2);
;         __builtin_amdgcn_global_load_lds((const unsigned*)(s0 + ntot), (PG8_LAS unsigned*)(lds0 + stage + 8192 + wid * 1024), 16, 0, 2);
;     }
;     __device__ __forceinline__ void read(v4i_t& t0, v4i_t& t1, int tid, unsigned ldsb) const {
;         asm volatile("ds_read_b128 %0, %1" : "=&v"(t0) : "v"(ldsb + stage + 16u * (unsigned)tid) : "memory");
;         asm volatile("ds_read_b128 %0, %1" : "=&v"(t1) : "v"(ldsb + stage + 8192u + 16u * (unsigned)tid) : "memory");
;     }
;     __device__ __forceinline__ void finish(v4i_t& t0, v4i_t& t1, int j, int tid) const {
;         asm volatile("" : "+v"(t0), "+v"(t1));
;         const float* s0; unsigned char* d; addr(j, tid, s0, d);
;         const f32x4 r0 = __builtin_bit_cast(f32x4, t0) * 64.f, r1 = __builtin_bit_cast(f32x4, t1) * 64.f;
;         int w0 = 0, w1 = 0; w0 = __builtin_amdgcn_cvt_pk_fp8_f32(r0[0], r1[0], w0, false); w0 = __builtin_amdgcn_cvt_pk_fp8_f32(r0[1], r1[1], w0, true);
;         w1 = __builtin_amdgcn_cvt_pk_fp8_f32(r0[2], r1[2], w1, false); w1 = __builtin_amdgcn_cvt_pk_fp8_f32(r0[3], r1[3], w1, true);
;         typedef int v2is __attribute__((ext_vector_type(2))); __builtin_nontemporal_store((v2is){w0, w1}, (v2is*)d);
.Lp4vg_wd_a1:
	s_waitcnt lgkmcnt(0)
	s_barrier
	s_cmp_lt_i32 s98, 0
	s_cbranch_scc1 .Lp4vg_mmslow_a
	s_cmp_gt_i32 s42, 31
	s_cbranch_scc1 .Lp4vg_mmslow_a
	s_setprio 1
	s_waitcnt lgkmcnt(0)
	v_mfma_f32_16x16x32_bf16 v[138:141], v[158:161], v[198:201], v[138:141]
	s_add_i32 s22, s98, s47
	s_lshr_b32 s23, s22, 1
	v_mfma_f32_16x16x32_bf16 v[134:137], v[166:169], v[198:201], v[134:137]
	s_and_b32 s22, s22, 1
	s_lshl_b32 s22, s22, 12
	v_mfma_f32_16x16x32_bf16 v[126:129], v[158:161], v[190:193], v[126:129]
	s_mulk_i32 s23, 0x2100
	s_add_i32 s22, s22, s23
	v_mfma_f32_16x16x32_bf16 v[122:125], v[166:169], v[190:193], v[122:125]
	v_mul_f32_e32 v6, s2, v6
	v_mul_f32_e32 v10, s2, v10
	v_mfma_f32_16x16x32_bf16 v[110:113], v[158:161], v[182:185], v[110:113]
	v_mul_f32_e32 v7, s2, v7
	v_mul_f32_e32 v11, s2, v11
	v_mfma_f32_16x16x32_bf16 v[106:109], v[166:169], v[182:185], v[106:109]
	v_cvt_pk_fp8_f32 v6, v6, v10
	v_mul_f32_e32 v8, s2, v8
	v_mfma_f32_16x16x32_bf16 v[94:97], v[158:161], v[174:177], v[94:97]
	v_mul_f32_e32 v12, s2, v12
	v_cvt_pk_fp8_f32 v6, v7, v11 op_sel:[0,0,1]
	v_mfma_f32_16x16x32_bf16 v[90:93], v[166:169], v[174:177], v[90:93]
	v_mul_f32_e32 v9, s2, v9
	v_mul_f32_e32 v13, s2, v13
	v_mfma_f32_16x16x32_bf16 v[138:141], v[162:165], v[202:205], v[138:141]
	v_readlane_b32 s4, v251, 49
	v_cvt_pk_fp8_f32 v7, v8, v12
	v_mfma_f32_16x16x32_bf16 v[134:137], v[170:173], v[202:205], v[134:137]
	v_readlane_b32 s5, v251, 31
	v_cvt_pk_fp8_f32 v7, v9, v13 op_sel:[0,0,1]
	v_mfma_f32_16x16x32_bf16 v[126:129], v[162:165], v[194:197], v[126:129]
	s_add_u32 s4, s4, s22
	s_addc_u32 s5, s5, 0
	v_mfma_f32_16x16x32_bf16 v[122:125], v[170:173], v[194:197], v[122:125]
	v_lshlrev_b32_e32 v4, 1, v208
	global_store_dwordx2 v4, v[6:7], s[4:5] nt
	v_mfma_f32_16x16x32_bf16 v[110:113], v[162:165], v[186:189], v[110:113]
	s_add_i32 s22, s42, s47
	s_lshr_b32 s23, s22, 1
	v_mfma_f32_16x16x32_bf16 v[106:109], v[170:173], v[186:189], v[106:109]
	s_and_b32 s22, s22, 1
	s_lshl_b32 s22, s22, 13
	v_mfma_f32_16x16x32_bf16 v[94:97], v[162:165], v[178:181], v[94:97]
	s_lshl_b32 s23, s23, 15
	s_add_i32 s22, s22, s23
	v_mfma_f32_16x16x32_bf16 v[90:93], v[170:173], v[178:181], v[90:93]
	s_setprio 0
	s_setprio 1
	v_readlane_b32 s4, v251, 36
	v_readlane_b32 s5, v251, 37
	v_mfma_f32_16x16x32_bf16 v[130:133], v[142:145], v[198:201], v[130:133]
	s_add_u32 s4, s4, s22
	s_addc_u32 s5, s5, 0
	v_mfma_f32_16x16x32_bf16 v[118:121], v[150:153], v[198:201], v[118:121]
	s_add_u32 s34, s4, s8
	s_addc_u32 s35, s5, s9
	v_mfma_f32_16x16x32_bf16 v[114:117], v[142:145], v[190:193], v[114:117]
	v_lshlrev_b32_e32 v2, 2, v208
	global_load_dwordx4 v[6:9], v2, s[4:5] nt
	v_mfma_f32_16x16x32_bf16 v[102:105], v[150:153], v[190:193], v[102:105]
	global_load_dwordx4 v[10:13], v2, s[34:35] nt
	s_mov_b32 s100, 3
	v_mfma_f32_16x16x32_bf16 v[98:101], v[142:145], v[182:185], v[98:101]
	s_mov_b32 s98, s42
	s_add_i32 s42, s42, 1
	v_mfma_f32_16x16x32_bf16 v[86:89], v[150:153], v[182:185], v[86:89]
	s_add_u32 s4, s24, 0xfff80080
	s_addc_u32 s5, s25, -1
	v_mfma_f32_16x16x32_bf16 v[82:85], v[142:145], v[174:177], v[82:85]
	s_cmp_eq_u32 s60, 28
	s_cselect_b32 s5, s11, s5
	s_cselect_b32 s4, s56, s4
	s_cselect_b32 s35, s15, s59
	s_cselect_b32 s34, s57, s58
	v_mfma_f32_16x16x32_bf16 v[78:81], v[150:153], v[174:177], v[78:81]
	v_mfma_f32_16x16x32_bf16 v[130:133], v[146:149], v[202:205], v[130:133]
	v_mfma_f32_16x16x32_bf16 v[118:121], v[154:157], v[202:205], v[118:121]
	v_mfma_f32_16x16x32_bf16 v[114:117], v[146:149], v[194:197], v[114:117]
	v_mfma_f32_16x16x32_bf16 v[102:105], v[154:157], v[194:197], v[102:105]
	v_mfma_f32_16x16x32_bf16 v[98:101], v[146:149], v[186:189], v[98:101]
	v_mfma_f32_16x16x32_bf16 v[86:89], v[154:157], v[186:189], v[86:89]
	v_mfma_f32_16x16x32_bf16 v[82:85], v[146:149], v[178:181], v[82:85]
	v_mfma_f32_16x16x32_bf16 v[78:81], v[154:157], v[178:181], v[78:81]
	s_setprio 0
	s_branch .Lp4vg_mmjoin_a

; #define PG8_LAS __attribute__((address_space(3)))
;     __device__ __forceinline__ void issue(PG8_LAS unsigned char* lds0, int j, int tid, int wid) const {
;         const float* s0; unsigned char* d; addr(j, tid, s0, d);
;         __builtin_amdgcn_global_load_lds((const unsigned*)s0, (PG8_LAS unsigned*)(lds0 + stage + wid * 1024), 16, 0, 2);
;         __builtin_amdgcn_global_load_lds((const unsigned*)(s0 + ntot), (PG8_LAS unsigned*)(lds0 + stage + 8192 + wid * 1024), 16, 0, 2);
;     }
;     __device__ __forceinline__ void read(v4i_t& t0, v4i_t& t1, int tid, unsigned ldsb) const {
;         asm volatile("ds_read_b128 %0, %1" : "=&v"(t0) : "v"(ldsb + stage + 16u * (unsigned)tid) : "memory");
;         asm volatile("ds_read_b128 %0, %1" : "=&v"(t1) : "v"(ldsb + stage + 8192u + 16u * (unsigned)tid) : "memory");
;     }
;     __device__ __forceinline__ void finish(v4i_t& t0, v4i_t& t1, int j, int tid) const {
;         asm volatile("" : "+v"(t0), "+v"(t1));
;         const float* s0; unsigned char* d; addr(j, tid, s0, d);
;         const f32x4 r0 = __builtin_bit_cast(f32x4, t0) * 64.f, r1 = __builtin_bit_cast(f32x4, t1) * 64.f;
;         int w0 = 0, w1 = 0; w0 = __builtin_amdgcn_cvt_pk_fp8_f32(r0[0], r1[0], w0, false); w0 = __builtin_amdgcn_cvt_pk_fp8_f32(r0[1], r1[1], w0, true);
;         w1 = __builtin_amdgcn_cvt_pk_fp8_f32(r0[2], r1[2], w1, false); w1 = __builtin_amdgcn_cvt_pk_fp8_f32(r0[3], r1[3], w1, true);
;         typedef int v2is __attribute__((ext_vector_type(2))); __builtin_nontemporal_store((v2is){w0, w1}, (v2is*)d);
.Lp4vg_wd_b1:
	s_waitcnt lgkmcnt(0)
	s_cmp_lt_i32 s99, 0
	s_cbranch_scc1 .Lp4vg_mmslow_b
	s_cmp_gt_i32 s42, 31
	s_cbranch_scc1 .Lp4vg_mmslow_b
	s_barrier
	s_setprio 1
	s_waitcnt lgkmcnt(0)
	v_mfma_f32_16x16x32_bf16 v[138:141], v[158:161], v[198:201], v[138:141]
	s_add_i32 s22, s99, s47
	s_lshr_b32 s23, s22, 1
	v_mfma_f32_16x16x32_bf16 v[134:137], v[166:169], v[198:201], v[134:137]
	s_and_b32 s22, s22, 1
	s_lshl_b32 s22, s22, 12
	v_mfma_f32_16x16x32_bf16 v[126:129], v[158:161], v[190:193], v[126:129]
	s_mulk_i32 s23, 0x2100
	s_add_i32 s22, s22, s23
	v_mfma_f32_16x16x32_bf16 v[122:125], v[166:169], v[190:193], v[122:125]
	v_mul_f32_e32 v242, s2, v242
	v_mul_f32_e32 v246, s2, v246
	v_mfma_f32_16x16x32_bf16 v[110:113], v[158:161], v[182:185], v[110:113]
	v_mul_f32_e32 v243, s2, v243
	v_mul_f32_e32 v247, s2, v247
	v_mfma_f32_16x16x32_bf16 v[106:109], v[166:169], v[182:185], v[106:109]
	v_cvt_pk_fp8_f32 v242, v242, v246
	v_mul_f32_e32 v244, s2, v244
	v_mfma_f32_16x16x32_bf16 v[94:97], v[158:161], v[174:177], v[94:97]
	v_mul_f32_e32 v248, s2, v248
	v_cvt_pk_fp8_f32 v242, v243, v247 op_sel:[0,0,1]
	v_mfma_f32_16x16x32_bf16 v[90:93], v[166:169], v[174:177], v[90:93]
	v_mul_f32_e32 v245, s2, v245
	v_mul_f32_e32 v249, s2, v249
	v_mfma_f32_16x16x32_bf16 v[138:141], v[162:165], v[202:205], v[138:141]
	v_readlane_b32 s4, v251, 49
	v_cvt_pk_fp8_f32 v243, v244, v248
	v_mfma_f32_16x16x32_bf16 v[134:137], v[170:173], v[202:205], v[134:137]
	v_readlane_b32 s5, v251, 31
	v_cvt_pk_fp8_f32 v243, v245, v249 op_sel:[0,0,1]
	v_mfma_f32_16x16x32_bf16 v[126:129], v[162:165], v[194:197], v[126:129]
	s_add_u32 s4, s4, s22
	s_addc_u32 s5, s5, 0
	v_mfma_f32_16x16x32_bf16 v[122:125], v[170:173], v[194:197], v[122:125]
	v_lshlrev_b32_e32 v232, 1, v208
	global_store_dwordx2 v232, v[242:243], s[4:5] nt
	v_mfma_f32_16x16x32_bf16 v[110:113], v[162:165], v[186:189], v[110:113]
	s_add_i32 s22, s42, s47
	s_lshr_b32 s23, s22, 1
	v_mfma_f32_16x16x32_bf16 v[106:109], v[170:173], v[186:189], v[106:109]
	s_and_b32 s22, s22, 1
	s_lshl_b32 s22, s22, 13
	v_mfma_f32_16x16x32_bf16 v[94:97], v[162:165], v[178:181], v[94:97]
	s_lshl_b32 s23, s23, 15
	s_add_i32 s22, s22, s23
	v_mfma_f32_16x16x32_bf16 v[90:93], v[170:173], v[178:181], v[90:93]
	s_setprio 0
	s_setprio 1
	v_readlane_b32 s4, v251, 36
	v_readlane_b32 s5, v251, 37
	v_mfma_f32_16x16x32_bf16 v[130:133], v[142:145], v[198:201], v[130:133]
	s_add_u32 s4, s4, s22
	s_addc_u32 s5, s5, 0
	v_mfma_f32_16x16x32_bf16 v[118:121], v[150:153], v[198:201], v[118:121]
	s_add_u32 s64, s4, s8
	s_addc_u32 s65, s5, s9
	v_mfma_f32_16x16x32_bf16 v[114:117], v[142:145], v[190:193], v[114:117]
	v_lshlrev_b32_e32 v2, 2, v208
	global_load_dwordx4 v[242:245], v2, s[4:5] nt
	v_mfma_f32_16x16x32_bf16 v[102:105], v[150:153], v[190:193], v[102:105]
	global_load_dwordx4 v[246:249], v2, s[64:65] nt
	s_mov_b32 s100, 3
	v_mfma_f32_16x16x32_bf16 v[98:101], v[142:145], v[182:185], v[98:101]
	s_mov_b32 s99, s42
	s_add_i32 s42, s42, 1
	v_mfma_f32_16x16x32_bf16 v[86:89], v[150:153], v[182:185], v[86:89]
	v_mfma_f32_16x16x32_bf16 v[82:85], v[142:145], v[174:177], v[82:85]
	v_mfma_f32_16x16x32_bf16 v[78:81], v[150:153], v[174:177], v[78:81]
	v_mfma_f32_16x16x32_bf16 v[130:133], v[146:149], v[202:205], v[130:133]
	v_mfma_f32_16x16x32_bf16 v[118:121], v[154:157], v[202:205], v[118:121]
	v_mfma_f32_16x16x32_bf16 v[114:117], v[146:149], v[194:197], v[114:117]
	v_mfma_f32_16x16x32_bf16 v[102:105], v[154:157], v[194:197], v[102:105]
	v_mfma_f32_16x16x32_bf16 v[98:101], v[146:149], v[186:189], v[98:101]
	v_mfma_f32_16x16x32_bf16 v[86:89], v[154:157], v[186:189], v[86:89]
	v_mfma_f32_16x16x32_bf16 v[82:85], v[146:149], v[178:181], v[82:85]
	v_mfma_f32_16x16x32_bf16 v[78:81], v[154:157], v[178:181], v[78:81]
	s_setprio 0
	s_branch .Lp4vg_mmafter_b
